# pool unit: the four per-channel scale loads of an output tile issued together before the MFMAs (were serialized load+wait x4); MFMA->VALU pad re-derived
# baseline (speedup 1.0000x reference)
.LBB0_609:
	v_or_b32_e32 v2, s94, v96
	v_mad_u32_u24 v113, v2, s35, v97
	ds_read_b128 v[2:5], v113
	ds_read_b128 v[114:117], v113 offset:32
	v_lshl_add_u64 v[118:119], s[94:95], 2, v[42:43]
	global_load_dwordx4 v[156:159], v[118:119], off
	global_load_dwordx4 v[160:163], v[118:119], off offset:32
	global_load_dwordx4 v[164:167], v[118:119], off offset:64
	global_load_dwordx4 v[168:171], v[118:119], off offset:96
	s_and_b64 vcc, exec, s[26:27]
	s_mov_b64 s[26:27], 0
	s_waitcnt lgkmcnt(1)
	v_mfma_f32_32x32x16_bf16 v[2:17], v[2:5], v[18:21], 0
	s_waitcnt lgkmcnt(0)
	v_mfma_f32_32x32x16_bf16 v[2:17], v[114:117], v[22:25], v[2:17]
	ds_read_b128 v[114:117], v113 offset:64
	s_waitcnt lgkmcnt(0)
	v_mfma_f32_32x32x16_bf16 v[2:17], v[114:117], v[26:29], v[2:17]
	ds_read_b128 v[114:117], v113 offset:96
	v_add_u32_e32 v113, s94, v98
	v_lshl_add_u32 v113, v113, 1, v95
	s_mov_b32 s94, 32
	s_waitcnt lgkmcnt(0)
	v_mfma_f32_32x32x16_bf16 v[2:17], v[114:117], v[30:33], v[2:17]
	s_waitcnt vmcnt(0)
	s_nop 10
	v_pk_mul_f32 v[2:3], v[2:3], v[156:157]
	s_nop 0
	v_cvt_pk_bf16_f32 v114, v2, v3
	v_pk_mul_f32 v[2:3], v[4:5], v[158:159]
	s_nop 0
	v_cvt_pk_bf16_f32 v115, v2, v3
	v_pk_mul_f32 v[2:3], v[6:7], v[160:161]
	v_pk_mul_f32 v[4:5], v[8:9], v[162:163]
	v_cvt_pk_bf16_f32 v2, v2, v3
	v_cvt_pk_bf16_f32 v3, v4, v5
	ds_write2_b64 v113, v[114:115], v[2:3] offset1:2
	v_pk_mul_f32 v[2:3], v[10:11], v[164:165]
	s_nop 0
	v_cvt_pk_bf16_f32 v6, v2, v3
	v_pk_mul_f32 v[2:3], v[12:13], v[166:167]
	s_nop 0
	v_cvt_pk_bf16_f32 v7, v2, v3
	v_pk_mul_f32 v[2:3], v[14:15], v[168:169]
	v_pk_mul_f32 v[4:5], v[16:17], v[170:171]
	v_cvt_pk_bf16_f32 v2, v2, v3
	v_cvt_pk_bf16_f32 v3, v4, v5
	ds_write2_b64 v113, v[6:7], v[2:3] offset0:4 offset1:6
	s_cbranch_vccnz .LBB0_609
	s_waitcnt lgkmcnt(0)
	s_barrier
	ds_read_b128 v[2:5], v110
	v_add_u32_e32 v6, s36, v48
	v_ashrrev_i32_e32 v7, 31, v6
	v_lshlrev_b64 v[6:7], 10, v[6:7]
	v_lshl_add_u64 v[6:7], v[44:45], 0, v[6:7]
	s_waitcnt lgkmcnt(0)
	global_store_dwordx4 v[6:7], v[2:5], off
	ds_read_b128 v[2:5], v111
	v_add_u32_e32 v6, s36, v49
	v_ashrrev_i32_e32 v7, 31, v6
	v_lshlrev_b64 v[6:7], 10, v[6:7]
	v_lshl_add_u64 v[6:7], v[44:45], 0, v[6:7]
	s_waitcnt lgkmcnt(0)
	global_store_dwordx4 v[6:7], v[2:5], off
	ds_read_b128 v[2:5], v112
	v_add_u32_e32 v6, s36, v50
	v_ashrrev_i32_e32 v7, 31, v6
	v_lshlrev_b64 v[6:7], 10, v[6:7]
	v_lshl_add_u64 v[6:7], v[44:45], 0, v[6:7]
	s_waitcnt lgkmcnt(0)
	global_store_dwordx4 v[6:7], v[2:5], off
	ds_read_b128 v[2:5], v0
	v_add_u32_e32 v6, s36, v51
	v_ashrrev_i32_e32 v7, 31, v6
	v_lshlrev_b64 v[6:7], 10, v[6:7]
	s_add_i32 s5, s5, s76
	v_lshl_add_u64 v[6:7], v[44:45], 0, v[6:7]
	s_cmpk_lt_i32 s5, 0x100
	s_waitcnt lgkmcnt(0)
	global_store_dwordx4 v[6:7], v[2:5], off
	s_barrier
	s_cbranch_scc1 .LBB0_595
